# WIN phase: workgroups that own 6 of the 6.5/6.75 rounds of tiles start 4x s_sleep 127 later so their epilogue store bursts fall between those of the 7-tile workgroups
# baseline (speedup 1.0000x reference)
;   __device__ __forceinline__ bool next(int i,AttnUnit&u)const{ const int v=vcu+(i>>2)*grid; if(v>=256)return false; const int k=i&3,s=v&7; u.bh=v>>3; u.qb=(k==0)?s:(k==1)?15-s:(k==2)?16+s:31-s; return true; }
; #define REP(n) for (int rep_ = 0; rep_ < 1 + MK_REPN * (((MK_DUP) >> (n)) & 1); ++rep_)
; #define PHASE_BEGIN() do { int t_ = threadIdx.x; asm volatile("" : "+v"(t_)); F.tid = t_; F.lane = t_ & 63; F.wave = __builtin_amdgcn_readfirstlane(t_ >> 6); \
;         A = (KArgs)__builtin_amdgcn_kernarg_segment_ptr(); asm volatile("" : "+s"(A)); ws = A->ws; F.ws = ws; F.ctl = (gu32*)(ws + WS_CTL); } while (0)
; #define SEAM(k) do { if (IN(k) && IN((k) + 1)) xcd_barrier(bar); } while (0)
;     __device__ __forceinline__ bool next(int i, Unit& u) const {
;         const int nwin = 128 * 13; const long L0 = (long)i * G + c; if (L0 >= nwin + nkv) return false;
;         int L = (int)L0;
;         if (L < nwin) { int wgid = L; { const int q = nwin / 8, xcd = wgid % 8, off = wgid / 8; wgid = xcd * q + off; }
;             const int nig = 8 * 13, gid = wgid / nig, fm = gid * 8; u.pm = TILE_X + fm + ((wgid % nig) % 8); u.pn = tin + (wgid % nig) / 8; return true; }
;         L -= nwin; const int ty = L >> 4, a = (L >> 2) & 3, b = L & 3, l = ty & 1;
;         if (ty < 2) { u.pm = TILE_MK + a; u.pn = TILE_MK + 4 + 8 * l + b; } else { u.pm = TILE_MK + 8 + 8 * l + a; u.pn = TILE_MK + b; }
;         return true;
;     }
; __global__ void __launch_bounds__(NWAVES * 64, 2) mk_fwd(Args args) {
;     ...
;         if (EN(4) && IN(pb + 2)) { PHASE_BEGIN(); unsigned char* wl = ws + WS_W + (size_t)l * W_LAYER;
;             pg8::Gemm g{(const bf16*)ws, (const bf16*)ws, M, NINP, D}; const pg8::WinKVOrder S{F.G, (int)blockIdx.x, (int)((WS_W + (size_t)l * W_LAYER + WO_IN) >> 19), l == 0 ? 64 : 0};
;             const pg8::EpiWinKV E{ws, SSV(4 * l + 1), QSCALE, (int)((WS_W + (size_t)l * W_LAYER + WO_IN) >> 19)};
;             REP(4) pg8::gemm_phase<pg8::EpiWinKV, pg8::WinKVOrder, true, true>(F.lds + RING_OFF, g, S, E); SEAM(pb + 2);
.LBB0_583:
	s_andn2_b64 vcc, exec, s[4:5]
	v_writelane_b32 v252, s89, 27
	s_cbranch_vccnz .LBB0_936
	v_mov_b32_e32 v1, v0
	s_mov_b64 s[4:5], s[66:67]
	v_readlane_b32 s11, v252, 18
	s_nop 0
	s_cmp_eq_u32 s11, 0
	s_cselect_b32 s11, 64, 0
	s_add_i32 s11, s11, 0x80
	s_cmp_lt_u32 s2, s11
	s_cbranch_scc1 .Lwinstag_skip
	s_sleep 127
	s_sleep 127
	s_sleep 127
	s_sleep 127
